# adds attention units: static s_setprio 1 for waves 4-7 (staggers the two waves of each SIMD inside the per-tile barrier interval)
# baseline (speedup 1.0000x reference)
.LBB0_362:
	s_setprio 0
	v_mov_b32_e32 v1, v0
	s_waitcnt vmcnt(0)
	v_cmp_eq_u32_e32 vcc, 0, v1
	s_barrier
	s_and_saveexec_b64 s[0:1], vcc
	s_cbranch_execz .LBB0_366
	s_mov_b64 s[6:7], exec
	v_mbcnt_lo_u32_b32 v1, s6, 0
	v_mbcnt_hi_u32_b32 v1, s7, v1
	v_cmp_eq_u32_e32 vcc, 0, v1
	s_and_saveexec_b64 s[4:5], vcc
	s_cbranch_execz .LBB0_365
	s_bcnt1_i32_b64 s6, s[6:7]
	v_mov_b32_e32 v2, s6
	v_readlane_b32 s6, v236, 20
	v_readlane_b32 s7, v236, 21
	s_nop 4
	global_atomic_add v2, v3, v2, s[6:7] sc0

.LBB0_522:
	s_or_b64 exec, exec, s[0:1]
	s_cmpk_gt_u32 s8, 0xff
	s_cbranch_scc0 .Lattn_prio_done
	s_setprio 1
.Lattn_prio_done:
	s_lshl_b32 s0, s9, 8
	s_lshl_b32 s4, s11, 12
	v_and_b32_e32 v5, 31, v4
	s_add_i32 s0, s4, s0
	v_ashrrev_i32_e32 v28, 3, v4
	s_ashr_i32 s1, s8, 1
	v_or_b32_e32 v1, s0, v5
	v_add_u32_e32 v2, s4, v28
	s_lshl_b32 s0, s10, 7
	s_andn2_b32 s1, s1, 31
	v_mul_lo_u32 v2, v2, s90
	s_and_b32 s0, s0, 0x380
	v_add_u32_e32 v1, s1, v1
	v_lshl_add_u64 v[6:7], v[2:3], 1, s[68:69]
	s_lshl_b32 s14, s0, 1
	v_lshlrev_b32_e32 v2, 5, v4
	v_and_b32_e32 v2, 0xe0, v2
	v_lshl_add_u64 v[6:7], v[6:7], 0, s[14:15]
	v_mul_lo_u32 v24, v1, s90
	v_mov_b32_e32 v25, v3
	v_bfe_u32 v30, v4, 5, 1
	v_lshl_add_u64 v[22:23], v[6:7], 0, v[2:3]
	s_mov_b64 s[4:5], 0x2000
	s_movk_i32 s1, 0x2000
	v_lshl_add_u64 v[164:165], v[24:25], 1, s[68:69]
	v_lshl_add_u64 v[166:167], v[22:23], 0, s[4:5]
	s_mov_b64 s[4:5], 0x2800
	v_add_co_u32_e32 v10, vcc, s1, v22
	v_lshl_add_u64 v[24:25], v[164:165], 0, s[14:15]
	v_lshlrev_b32_e32 v170, 4, v30
	v_mov_b32_e32 v171, v3
	v_lshl_add_u64 v[168:169], v[22:23], 0, s[4:5]
	v_addc_co_u32_e32 v11, vcc, 0, v23, vcc
	v_lshl_add_u64 v[24:25], v[24:25], 0, v[170:171]
	s_mov_b64 s[4:5], 0x1800
	s_movk_i32 s1, 0x1000
	v_lshl_add_u64 v[26:27], v[24:25], 0, s[4:5]
	v_add_co_u32_e32 v24, vcc, s1, v24
	s_movk_i32 s1, 0x110
	s_barrier
	global_load_dwordx4 v[6:9], v[10:11], off
	s_nop 0
	global_load_dwordx4 v[10:13], v[10:11], off offset:2048
	s_nop 0
	global_load_dwordx4 v[14:17], v[166:167], off offset:16
	global_load_dwordx4 v[18:21], v[168:169], off offset:16
	global_load_dwordx4 v[100:103], v[26:27], off offset:32
	global_load_dwordx4 v[104:107], v[26:27], off offset:64
	global_load_dwordx4 v[108:111], v[26:27], off offset:96
	global_load_dwordx4 v[112:115], v[26:27], off offset:128
	global_load_dwordx4 v[116:119], v[26:27], off offset:160
	global_load_dwordx4 v[120:123], v[26:27], off offset:192
	global_load_dwordx4 v[124:127], v[26:27], off offset:224
	v_mul_lo_u32 v26, v28, s1
	s_movk_i32 s1, 0x140
	v_addc_co_u32_e32 v25, vcc, 0, v25, vcc
	v_add3_u32 v178, 0, v26, v2
	v_mul_lo_u32 v26, v28, s1
	s_mov_b64 s[4:5], 0x1d2000
	s_mov_b32 s1, 0x1d2000
	v_add3_u32 v179, 0, v26, v2
	v_lshl_add_u64 v[26:27], v[22:23], 0, s[4:5]
	v_add_co_u32_e32 v28, vcc, s1, v22
	s_mov_b64 s[4:5], 0x1d2800
	s_nop 0
	v_addc_co_u32_e32 v29, vcc, 0, v23, vcc
	v_lshl_add_u64 v[22:23], v[22:23], 0, s[4:5]
	v_readlane_b32 s4, v237, 18
	v_lshlrev_b32_e32 v2, 7, v1
	v_readlane_b32 s5, v237, 19
	global_load_dwordx4 v[136:139], v[28:29], off
	global_load_dwordx4 v[132:135], v[28:29], off offset:2048
	global_load_dwordx4 v[128:131], v[22:23], off offset:16
	v_lshl_add_u64 v[172:173], v[2:3], 2, s[4:5]
	global_load_dwordx2 v[176:177], v[172:173], off
	global_load_dwordx4 v[140:143], v[24:25], off offset:2048
	global_load_dwordx4 v[144:147], v[26:27], off offset:16
	v_lshrrev_b32_e32 v2, 2, v4
	v_and_b32_e32 v22, 16, v4
	v_lshlrev_b32_e32 v171, 2, v30
	v_and_or_b32 v2, v2, 3, v171
	v_mul_u32_u24_e32 v2, 0x140, v2
	v_mul_u32_u24_e32 v181, 0x110, v5
	v_mov_b32_e32 v5, v3
	s_lshl_b32 s5, s9, 2
	s_ashr_i32 s1, s8, 7
	s_mov_b32 s7, 0
	s_add_i32 s1, s1, s5
	s_add_i32 s4, s5, 4
	s_or_b32 s5, s5, 3
	v_mov_b32_e32 v184, 0xf149f2ca
	v_mov_b32_e32 v183, 0
	s_waitcnt vmcnt(16)
	ds_write_b128 v178, v[6:9]
	s_waitcnt vmcnt(14)
	ds_write_b128 v178, v[14:17] offset:16
	ds_write_b128 v179, v[10:13] offset:34816
	s_waitcnt vmcnt(13)
	ds_write_b128 v179, v[18:21] offset:34832
	v_lshlrev_b32_e32 v6, 2, v4
	v_and_or_b32 v6, v6, 12, v22
	v_lshlrev_b32_e32 v6, 1, v6
	v_add3_u32 v180, 0, v2, v6
	v_and_or_b32 v2, v4, 63, 32
	v_mov_b32_e32 v16, v3
	v_mov_b32_e32 v17, v3
	v_mul_u32_u24_e32 v182, 0x110, v2
	v_mov_b32_e32 v2, v3
	v_mov_b32_e32 v4, v3
	v_mov_b32_e32 v6, v3
	v_mov_b32_e32 v7, v3
	v_mov_b32_e32 v8, v3
	v_mov_b32_e32 v9, v3
	v_mov_b32_e32 v10, v3
	v_mov_b32_e32 v11, v3
	v_mov_b32_e32 v12, v3
	v_mov_b32_e32 v13, v3
	v_mov_b32_e32 v14, v3
	v_mov_b32_e32 v15, v3
	v_mov_b64_e32 v[66:67], v[16:17]
	v_mov_b64_e32 v[50:51], v[16:17]
	v_mov_b64_e32 v[34:35], v[16:17]
	v_mov_b64_e32 v[64:65], v[14:15]
	v_mov_b64_e32 v[62:63], v[12:13]
	v_mov_b64_e32 v[60:61], v[10:11]
	v_mov_b64_e32 v[58:59], v[8:9]
	v_mov_b64_e32 v[56:57], v[6:7]
	v_mov_b64_e32 v[54:55], v[4:5]
	v_mov_b64_e32 v[52:53], v[2:3]
	v_mov_b64_e32 v[48:49], v[14:15]
	v_mov_b64_e32 v[46:47], v[12:13]
	v_mov_b64_e32 v[44:45], v[10:11]
	v_mov_b64_e32 v[42:43], v[8:9]
	v_mov_b64_e32 v[40:41], v[6:7]
	v_mov_b64_e32 v[38:39], v[4:5]
	v_mov_b64_e32 v[36:37], v[2:3]
	v_mov_b64_e32 v[32:33], v[14:15]
	v_mov_b64_e32 v[30:31], v[12:13]
	v_mov_b64_e32 v[28:29], v[10:11]
	v_mov_b64_e32 v[26:27], v[8:9]
	v_mov_b64_e32 v[24:25], v[6:7]
	v_mov_b64_e32 v[22:23], v[4:5]
	v_mov_b64_e32 v[20:21], v[2:3]
	v_mov_b64_e32 v[18:19], v[16:17]
	v_mov_b64_e32 v[16:17], v[14:15]
	v_mov_b64_e32 v[14:15], v[12:13]
	v_mov_b64_e32 v[12:13], v[10:11]
	v_mov_b64_e32 v[10:11], v[8:9]
	v_mov_b64_e32 v[8:9], v[6:7]
	v_mov_b64_e32 v[6:7], v[4:5]
	v_mov_b64_e32 v[4:5], v[2:3]
	s_waitcnt lgkmcnt(0)
	s_barrier
